# baseline (speedup 1.0000x reference)
.Lk_first:
	ds_read_b128 v[130:133], v219 offset:32768
	ds_read_b128 v[134:137], v219 offset:33792
	ds_read_b128 v[138:141], v219 offset:34816
	ds_read_b128 v[142:145], v219 offset:35840
	ds_read_b128 v[178:181], v219 offset:49152
	ds_read_b128 v[182:185], v219 offset:50176
	ds_read_b128 v[186:189], v219 offset:51200
	ds_read_b128 v[190:193], v219 offset:52224
	ds_read_b128 v[146:149], v220
	ds_read_b128 v[150:153], v220 offset:1024
	ds_read_b128 v[154:157], v221
	ds_read_b128 v[158:161], v221 offset:1024
	ds_read_b128 v[162:165], v222
	ds_read_b128 v[166:169], v222 offset:1024
	ds_read_b128 v[170:173], v223
	ds_read_b128 v[174:177], v223 offset:1024
	s_add_i32 s12, s8, 1
	s_mov_b32 m0, s43
	v_readlane_b32 s9, v248, s12
	s_nop 1
	v_add_u32_e32 v251, s9, v249
	global_load_lds_dwordx4 v251, s[18:19]
	v_add_u32_e32 v251, s9, v250
	s_mov_b32 m0, s44
	s_nop 0
	global_load_lds_dwordx4 v251, s[18:19]
	s_waitcnt lgkmcnt(0)
	s_barrier
	s_setprio 1
	v_mfma_f32_16x16x32_f16 v[124:127], v[130:133], v[146:149], 0
	v_mfma_f32_16x16x32_f16 v[120:123], v[138:141], v[146:149], 0
	v_mfma_f32_16x16x32_f16 v[52:55], v[178:181], v[146:149], 0
	v_mfma_f32_16x16x32_f16 v[40:43], v[186:189], v[146:149], 0
	v_mfma_f32_16x16x32_f16 v[116:119], v[130:133], v[154:157], 0
	v_mfma_f32_16x16x32_f16 v[112:115], v[138:141], v[154:157], 0
	v_mfma_f32_16x16x32_f16 v[36:39], v[178:181], v[154:157], 0
	v_mfma_f32_16x16x32_f16 v[32:35], v[186:189], v[154:157], 0
	v_mfma_f32_16x16x32_f16 v[108:111], v[130:133], v[162:165], 0
	v_mfma_f32_16x16x32_f16 v[104:107], v[138:141], v[162:165], 0
	v_mfma_f32_16x16x32_f16 v[28:31], v[178:181], v[162:165], 0
	v_mfma_f32_16x16x32_f16 v[24:27], v[186:189], v[162:165], 0
	v_mfma_f32_16x16x32_f16 v[100:103], v[130:133], v[170:173], 0
	v_mfma_f32_16x16x32_f16 v[96:99], v[138:141], v[170:173], 0
	v_mfma_f32_16x16x32_f16 v[20:23], v[178:181], v[170:173], 0
	v_mfma_f32_16x16x32_f16 v[16:19], v[186:189], v[170:173], 0
	v_mfma_f32_16x16x32_f16 v[124:127], v[134:137], v[150:153], v[124:127]
	v_mfma_f32_16x16x32_f16 v[120:123], v[142:145], v[150:153], v[120:123]
	v_mfma_f32_16x16x32_f16 v[52:55], v[182:185], v[150:153], v[52:55]
	v_mfma_f32_16x16x32_f16 v[40:43], v[190:193], v[150:153], v[40:43]
	v_mfma_f32_16x16x32_f16 v[116:119], v[134:137], v[158:161], v[116:119]
	v_mfma_f32_16x16x32_f16 v[112:115], v[142:145], v[158:161], v[112:115]
	v_mfma_f32_16x16x32_f16 v[36:39], v[182:185], v[158:161], v[36:39]
	v_mfma_f32_16x16x32_f16 v[32:35], v[190:193], v[158:161], v[32:35]
	v_mfma_f32_16x16x32_f16 v[108:111], v[134:137], v[166:169], v[108:111]
	v_mfma_f32_16x16x32_f16 v[104:107], v[142:145], v[166:169], v[104:107]
	v_mfma_f32_16x16x32_f16 v[28:31], v[182:185], v[166:169], v[28:31]
	v_mfma_f32_16x16x32_f16 v[24:27], v[190:193], v[166:169], v[24:27]
	v_mfma_f32_16x16x32_f16 v[100:103], v[134:137], v[174:177], v[100:103]
	v_mfma_f32_16x16x32_f16 v[96:99], v[142:145], v[174:177], v[96:99]
	v_mfma_f32_16x16x32_f16 v[20:23], v[182:185], v[174:177], v[20:23]
	v_mfma_f32_16x16x32_f16 v[16:19], v[190:193], v[174:177], v[16:19]
	s_setprio 0
	s_barrier
	ds_read_b128 v[146:149], v220 offset:16384
	ds_read_b128 v[150:153], v220 offset:17408
	ds_read_b128 v[154:157], v221 offset:16384
	ds_read_b128 v[158:161], v221 offset:17408
	ds_read_b128 v[162:165], v222 offset:16384
	ds_read_b128 v[166:169], v222 offset:17408
	ds_read_b128 v[170:173], v223 offset:16384
	ds_read_b128 v[174:177], v223 offset:17408
	v_add_u32_e32 v129, s7, v128
	s_mov_b32 m0, s22
	v_add_u32_e32 v194, 0xffffff80, v129
	global_load_lds_dwordx4 v194, s[10:11]
	v_add_u32_e32 v194, 0x47f80, v129
	s_mov_b32 m0, s23
	s_add_i32 s9, s8, 2
	global_load_lds_dwordx4 v194, s[10:11]
	v_readlane_b32 s13, v248, s9
	s_mov_b32 m0, s21
	s_nop 1
	v_add_u32_e32 v194, s13, v206
	global_load_lds_dwordx4 v194, s[18:19]
	v_add_u32_e32 v194, s13, v213
	s_mov_b32 m0, s24
	s_nop 0
	global_load_lds_dwordx4 v194, s[18:19]
	s_mov_b32 m0, s25
	v_add_u32_e32 v194, 0x8ff80, v129
	global_load_lds_dwordx4 v194, s[10:11]
	v_add_u32_e32 v194, 0xd7f80, v129
	s_mov_b32 m0, s26
	s_nop 0
	global_load_lds_dwordx4 v194, s[10:11]
	s_waitcnt vmcnt(8) lgkmcnt(0)
	s_barrier
	s_setprio 1
	v_mfma_f32_16x16x32_f16 v[12:15], v[130:133], v[146:149], 0
	v_mfma_f32_16x16x32_f16 v[8:11], v[138:141], v[146:149], 0
	v_mfma_f32_16x16x32_f16 v[64:67], v[178:181], v[146:149], 0
	v_mfma_f32_16x16x32_f16 v[68:71], v[186:189], v[146:149], 0
	v_mfma_f32_16x16x32_f16 v[4:7], v[130:133], v[154:157], 0
	v_mfma_f32_16x16x32_f16 v[0:3], v[138:141], v[154:157], 0
	v_mfma_f32_16x16x32_f16 v[72:75], v[178:181], v[154:157], 0
	v_mfma_f32_16x16x32_f16 v[76:79], v[186:189], v[154:157], 0
	v_mfma_f32_16x16x32_f16 v[44:47], v[130:133], v[162:165], 0
	v_mfma_f32_16x16x32_f16 v[48:51], v[138:141], v[162:165], 0
	v_mfma_f32_16x16x32_f16 v[80:83], v[178:181], v[162:165], 0
	v_mfma_f32_16x16x32_f16 v[84:87], v[186:189], v[162:165], 0
	v_mfma_f32_16x16x32_f16 v[56:59], v[130:133], v[170:173], 0
	v_mfma_f32_16x16x32_f16 v[60:63], v[138:141], v[170:173], 0
	v_mfma_f32_16x16x32_f16 v[88:91], v[178:181], v[170:173], 0
	v_mfma_f32_16x16x32_f16 v[92:95], v[186:189], v[170:173], 0
	v_mfma_f32_16x16x32_f16 v[12:15], v[134:137], v[150:153], v[12:15]
	v_mfma_f32_16x16x32_f16 v[8:11], v[142:145], v[150:153], v[8:11]
	v_mfma_f32_16x16x32_f16 v[64:67], v[182:185], v[150:153], v[64:67]
	v_mfma_f32_16x16x32_f16 v[68:71], v[190:193], v[150:153], v[68:71]
	v_mfma_f32_16x16x32_f16 v[4:7], v[134:137], v[158:161], v[4:7]
	v_mfma_f32_16x16x32_f16 v[0:3], v[142:145], v[158:161], v[0:3]
	v_mfma_f32_16x16x32_f16 v[72:75], v[182:185], v[158:161], v[72:75]
	v_mfma_f32_16x16x32_f16 v[76:79], v[190:193], v[158:161], v[76:79]
	v_mfma_f32_16x16x32_f16 v[44:47], v[134:137], v[166:169], v[44:47]
	v_mfma_f32_16x16x32_f16 v[48:51], v[142:145], v[166:169], v[48:51]
	v_mfma_f32_16x16x32_f16 v[80:83], v[182:185], v[166:169], v[80:83]
	v_mfma_f32_16x16x32_f16 v[84:87], v[190:193], v[166:169], v[84:87]
	v_mfma_f32_16x16x32_f16 v[56:59], v[134:137], v[174:177], v[56:59]
	v_mfma_f32_16x16x32_f16 v[60:63], v[142:145], v[174:177], v[60:63]
	v_mfma_f32_16x16x32_f16 v[88:91], v[182:185], v[174:177], v[88:91]
	v_mfma_f32_16x16x32_f16 v[92:95], v[190:193], v[174:177], v[92:95]
	s_setprio 0
	s_barrier
	ds_read_b128 v[130:133], v224
	ds_read_b128 v[134:137], v224 offset:1024
	ds_read_b128 v[138:141], v224 offset:2048
	ds_read_b128 v[142:145], v224 offset:3072
	ds_read_b128 v[178:181], v229
	ds_read_b128 v[182:185], v229 offset:1024
	ds_read_b128 v[186:189], v229 offset:2048
	ds_read_b128 v[190:193], v229 offset:3072
	ds_read_b128 v[146:149], v225
	ds_read_b128 v[150:153], v225 offset:1024
	ds_read_b128 v[154:157], v226
	ds_read_b128 v[158:161], v226 offset:1024
	ds_read_b128 v[162:165], v227
	ds_read_b128 v[166:169], v227 offset:1024
	ds_read_b128 v[170:173], v228
	ds_read_b128 v[174:177], v228 offset:1024
	v_readlane_b32 s12, v248, s9
	s_mov_b32 m0, s27
	s_nop 1
	v_add_u32_e32 v251, s12, v249
	global_load_lds_dwordx4 v251, s[18:19]
	v_add_u32_e32 v251, s12, v250
	s_mov_b32 m0, s28
	s_nop 0
	global_load_lds_dwordx4 v251, s[18:19]
	s_waitcnt vmcnt(8) lgkmcnt(0)
	s_barrier
	s_setprio 1
	v_mfma_f32_16x16x32_f16 v[124:127], v[130:133], v[146:149], v[124:127]
	v_mfma_f32_16x16x32_f16 v[120:123], v[138:141], v[146:149], v[120:123]
	v_mfma_f32_16x16x32_f16 v[52:55], v[178:181], v[146:149], v[52:55]
	v_mfma_f32_16x16x32_f16 v[40:43], v[186:189], v[146:149], v[40:43]
	v_mfma_f32_16x16x32_f16 v[116:119], v[130:133], v[154:157], v[116:119]
	v_mfma_f32_16x16x32_f16 v[112:115], v[138:141], v[154:157], v[112:115]
	v_mfma_f32_16x16x32_f16 v[36:39], v[178:181], v[154:157], v[36:39]
	v_mfma_f32_16x16x32_f16 v[32:35], v[186:189], v[154:157], v[32:35]
	v_mfma_f32_16x16x32_f16 v[108:111], v[130:133], v[162:165], v[108:111]
	v_mfma_f32_16x16x32_f16 v[104:107], v[138:141], v[162:165], v[104:107]
	v_mfma_f32_16x16x32_f16 v[28:31], v[178:181], v[162:165], v[28:31]
	v_mfma_f32_16x16x32_f16 v[24:27], v[186:189], v[162:165], v[24:27]
	v_mfma_f32_16x16x32_f16 v[100:103], v[130:133], v[170:173], v[100:103]
	v_mfma_f32_16x16x32_f16 v[96:99], v[138:141], v[170:173], v[96:99]
	v_mfma_f32_16x16x32_f16 v[20:23], v[178:181], v[170:173], v[20:23]
	v_mfma_f32_16x16x32_f16 v[16:19], v[186:189], v[170:173], v[16:19]
	v_mfma_f32_16x16x32_f16 v[124:127], v[134:137], v[150:153], v[124:127]
	v_mfma_f32_16x16x32_f16 v[120:123], v[142:145], v[150:153], v[120:123]
	v_mfma_f32_16x16x32_f16 v[52:55], v[182:185], v[150:153], v[52:55]
	v_mfma_f32_16x16x32_f16 v[40:43], v[190:193], v[150:153], v[40:43]
	v_mfma_f32_16x16x32_f16 v[116:119], v[134:137], v[158:161], v[116:119]
	v_mfma_f32_16x16x32_f16 v[112:115], v[142:145], v[158:161], v[112:115]
	v_mfma_f32_16x16x32_f16 v[36:39], v[182:185], v[158:161], v[36:39]
	v_mfma_f32_16x16x32_f16 v[32:35], v[190:193], v[158:161], v[32:35]
	v_mfma_f32_16x16x32_f16 v[108:111], v[134:137], v[166:169], v[108:111]
	v_mfma_f32_16x16x32_f16 v[104:107], v[142:145], v[166:169], v[104:107]
	v_mfma_f32_16x16x32_f16 v[28:31], v[182:185], v[166:169], v[28:31]
	v_mfma_f32_16x16x32_f16 v[24:27], v[190:193], v[166:169], v[24:27]
	v_mfma_f32_16x16x32_f16 v[100:103], v[134:137], v[174:177], v[100:103]
	v_mfma_f32_16x16x32_f16 v[96:99], v[142:145], v[174:177], v[96:99]
	v_mfma_f32_16x16x32_f16 v[20:23], v[182:185], v[174:177], v[20:23]
	v_mfma_f32_16x16x32_f16 v[16:19], v[190:193], v[174:177], v[16:19]
	s_setprio 0
	s_barrier
	ds_read_b128 v[146:149], v230
	ds_read_b128 v[150:153], v230 offset:1024
	ds_read_b128 v[154:157], v231
	ds_read_b128 v[158:161], v231 offset:1024
	ds_read_b128 v[162:165], v232
	ds_read_b128 v[166:169], v232 offset:1024
	ds_read_b128 v[170:173], v233
	ds_read_b128 v[174:177], v233 offset:1024
	s_mov_b32 m0, s37
	v_add_u32_e32 v194, 0x48000, v129
	global_load_lds_dwordx4 v129, s[10:11]
	s_mov_b32 m0, s38
	s_add_i32 s12, s8, 3
	global_load_lds_dwordx4 v194, s[10:11]
	v_readlane_b32 s13, v248, s12
	s_mov_b32 m0, s39
	s_nop 1
	v_add_u32_e32 v194, s13, v206
	global_load_lds_dwordx4 v194, s[18:19]
	v_add_u32_e32 v194, s13, v213
	s_mov_b32 m0, s40
	s_nop 0
	global_load_lds_dwordx4 v194, s[18:19]
	s_mov_b32 m0, s41
	v_add_u32_e32 v194, 0x90000, v129
	global_load_lds_dwordx4 v194, s[10:11]
	v_add_u32_e32 v194, 0xd8000, v129
	s_mov_b32 m0, s42
	s_nop 0
	global_load_lds_dwordx4 v194, s[10:11]
	s_waitcnt vmcnt(8) lgkmcnt(0)
	s_barrier
	s_setprio 1
	v_mfma_f32_16x16x32_f16 v[12:15], v[130:133], v[146:149], v[12:15]
	v_mfma_f32_16x16x32_f16 v[8:11], v[138:141], v[146:149], v[8:11]
	v_mfma_f32_16x16x32_f16 v[64:67], v[178:181], v[146:149], v[64:67]
	v_mfma_f32_16x16x32_f16 v[68:71], v[186:189], v[146:149], v[68:71]
	v_mfma_f32_16x16x32_f16 v[4:7], v[130:133], v[154:157], v[4:7]
	v_mfma_f32_16x16x32_f16 v[0:3], v[138:141], v[154:157], v[0:3]
	v_mfma_f32_16x16x32_f16 v[72:75], v[178:181], v[154:157], v[72:75]
	v_mfma_f32_16x16x32_f16 v[76:79], v[186:189], v[154:157], v[76:79]
	v_mfma_f32_16x16x32_f16 v[44:47], v[130:133], v[162:165], v[44:47]
	v_mfma_f32_16x16x32_f16 v[48:51], v[138:141], v[162:165], v[48:51]
	v_mfma_f32_16x16x32_f16 v[80:83], v[178:181], v[162:165], v[80:83]
	v_mfma_f32_16x16x32_f16 v[84:87], v[186:189], v[162:165], v[84:87]
	v_mfma_f32_16x16x32_f16 v[56:59], v[130:133], v[170:173], v[56:59]
	v_mfma_f32_16x16x32_f16 v[60:63], v[138:141], v[170:173], v[60:63]
	v_mfma_f32_16x16x32_f16 v[88:91], v[178:181], v[170:173], v[88:91]
	v_mfma_f32_16x16x32_f16 v[92:95], v[186:189], v[170:173], v[92:95]
	v_mfma_f32_16x16x32_f16 v[12:15], v[134:137], v[150:153], v[12:15]
	v_mfma_f32_16x16x32_f16 v[8:11], v[142:145], v[150:153], v[8:11]
	v_mfma_f32_16x16x32_f16 v[64:67], v[182:185], v[150:153], v[64:67]
	v_mfma_f32_16x16x32_f16 v[68:71], v[190:193], v[150:153], v[68:71]
	v_mfma_f32_16x16x32_f16 v[4:7], v[134:137], v[158:161], v[4:7]
	v_mfma_f32_16x16x32_f16 v[0:3], v[142:145], v[158:161], v[0:3]
	v_mfma_f32_16x16x32_f16 v[72:75], v[182:185], v[158:161], v[72:75]
	v_mfma_f32_16x16x32_f16 v[76:79], v[190:193], v[158:161], v[76:79]
	v_mfma_f32_16x16x32_f16 v[44:47], v[134:137], v[166:169], v[44:47]
	v_mfma_f32_16x16x32_f16 v[48:51], v[142:145], v[166:169], v[48:51]
	v_mfma_f32_16x16x32_f16 v[80:83], v[182:185], v[166:169], v[80:83]
	v_mfma_f32_16x16x32_f16 v[84:87], v[190:193], v[166:169], v[84:87]
	v_mfma_f32_16x16x32_f16 v[56:59], v[134:137], v[174:177], v[56:59]
	v_mfma_f32_16x16x32_f16 v[60:63], v[142:145], v[174:177], v[60:63]
	v_mfma_f32_16x16x32_f16 v[88:91], v[182:185], v[174:177], v[88:91]
	v_mfma_f32_16x16x32_f16 v[92:95], v[190:193], v[174:177], v[92:95]
	s_setprio 0
	s_addk_i32 s7, 0x100
	s_cmp_lt_u32 s8, 32
	s_mov_b32 s8, s9
	s_barrier
.LBB1_82:
	ds_read_b128 v[130:133], v219 offset:32768
	ds_read_b128 v[134:137], v219 offset:33792
	ds_read_b128 v[138:141], v219 offset:34816
	ds_read_b128 v[142:145], v219 offset:35840
	ds_read_b128 v[178:181], v219 offset:49152
	ds_read_b128 v[182:185], v219 offset:50176
	ds_read_b128 v[186:189], v219 offset:51200
	ds_read_b128 v[190:193], v219 offset:52224
	ds_read_b128 v[146:149], v220
	ds_read_b128 v[150:153], v220 offset:1024
	ds_read_b128 v[154:157], v221
	ds_read_b128 v[158:161], v221 offset:1024
	ds_read_b128 v[162:165], v222
	ds_read_b128 v[166:169], v222 offset:1024
	ds_read_b128 v[170:173], v223
	ds_read_b128 v[174:177], v223 offset:1024
	s_add_i32 s12, s8, 1
	s_mov_b32 m0, s43
	v_readlane_b32 s9, v248, s12
	s_nop 1
	v_add_u32_e32 v251, s9, v249
	global_load_lds_dwordx4 v251, s[18:19]
	v_add_u32_e32 v251, s9, v250
	s_mov_b32 m0, s44
	s_nop 0
	global_load_lds_dwordx4 v251, s[18:19]
	s_waitcnt vmcnt(8) lgkmcnt(0)
	s_barrier
	s_setprio 1
	v_mfma_f32_16x16x32_f16 v[124:127], v[130:133], v[146:149], v[124:127]
	v_mfma_f32_16x16x32_f16 v[120:123], v[138:141], v[146:149], v[120:123]
	v_mfma_f32_16x16x32_f16 v[52:55], v[178:181], v[146:149], v[52:55]
	v_mfma_f32_16x16x32_f16 v[40:43], v[186:189], v[146:149], v[40:43]
	v_mfma_f32_16x16x32_f16 v[116:119], v[130:133], v[154:157], v[116:119]
	v_mfma_f32_16x16x32_f16 v[112:115], v[138:141], v[154:157], v[112:115]
	v_mfma_f32_16x16x32_f16 v[36:39], v[178:181], v[154:157], v[36:39]
	v_mfma_f32_16x16x32_f16 v[32:35], v[186:189], v[154:157], v[32:35]
	v_mfma_f32_16x16x32_f16 v[108:111], v[130:133], v[162:165], v[108:111]
	v_mfma_f32_16x16x32_f16 v[104:107], v[138:141], v[162:165], v[104:107]
	v_mfma_f32_16x16x32_f16 v[28:31], v[178:181], v[162:165], v[28:31]
	v_mfma_f32_16x16x32_f16 v[24:27], v[186:189], v[162:165], v[24:27]
	v_mfma_f32_16x16x32_f16 v[100:103], v[130:133], v[170:173], v[100:103]
	v_mfma_f32_16x16x32_f16 v[96:99], v[138:141], v[170:173], v[96:99]
	v_mfma_f32_16x16x32_f16 v[20:23], v[178:181], v[170:173], v[20:23]
	v_mfma_f32_16x16x32_f16 v[16:19], v[186:189], v[170:173], v[16:19]
	v_mfma_f32_16x16x32_f16 v[124:127], v[134:137], v[150:153], v[124:127]
	v_mfma_f32_16x16x32_f16 v[120:123], v[142:145], v[150:153], v[120:123]
	v_mfma_f32_16x16x32_f16 v[52:55], v[182:185], v[150:153], v[52:55]
	v_mfma_f32_16x16x32_f16 v[40:43], v[190:193], v[150:153], v[40:43]
	v_mfma_f32_16x16x32_f16 v[116:119], v[134:137], v[158:161], v[116:119]
	v_mfma_f32_16x16x32_f16 v[112:115], v[142:145], v[158:161], v[112:115]
	v_mfma_f32_16x16x32_f16 v[36:39], v[182:185], v[158:161], v[36:39]
	v_mfma_f32_16x16x32_f16 v[32:35], v[190:193], v[158:161], v[32:35]
	v_mfma_f32_16x16x32_f16 v[108:111], v[134:137], v[166:169], v[108:111]
	v_mfma_f32_16x16x32_f16 v[104:107], v[142:145], v[166:169], v[104:107]
	v_mfma_f32_16x16x32_f16 v[28:31], v[182:185], v[166:169], v[28:31]
	v_mfma_f32_16x16x32_f16 v[24:27], v[190:193], v[166:169], v[24:27]
	v_mfma_f32_16x16x32_f16 v[100:103], v[134:137], v[174:177], v[100:103]
	v_mfma_f32_16x16x32_f16 v[96:99], v[142:145], v[174:177], v[96:99]
	v_mfma_f32_16x16x32_f16 v[20:23], v[182:185], v[174:177], v[20:23]
	v_mfma_f32_16x16x32_f16 v[16:19], v[190:193], v[174:177], v[16:19]
	s_setprio 0
	s_barrier
	ds_read_b128 v[146:149], v220 offset:16384
	ds_read_b128 v[150:153], v220 offset:17408
	ds_read_b128 v[154:157], v221 offset:16384
	ds_read_b128 v[158:161], v221 offset:17408
	ds_read_b128 v[162:165], v222 offset:16384
	ds_read_b128 v[166:169], v222 offset:17408
	ds_read_b128 v[170:173], v223 offset:16384
	ds_read_b128 v[174:177], v223 offset:17408
	v_add_u32_e32 v129, s7, v128
	s_mov_b32 m0, s22
	v_add_u32_e32 v194, 0xffffff80, v129
	global_load_lds_dwordx4 v194, s[10:11]
	v_add_u32_e32 v194, 0x47f80, v129
	s_mov_b32 m0, s23
	s_add_i32 s9, s8, 2
	global_load_lds_dwordx4 v194, s[10:11]
	v_readlane_b32 s13, v248, s9
	s_mov_b32 m0, s21
	s_nop 1
	v_add_u32_e32 v194, s13, v206
	global_load_lds_dwordx4 v194, s[18:19]
	v_add_u32_e32 v194, s13, v213
	s_mov_b32 m0, s24
	s_nop 0
	global_load_lds_dwordx4 v194, s[18:19]
	s_mov_b32 m0, s25
	v_add_u32_e32 v194, 0x8ff80, v129
	global_load_lds_dwordx4 v194, s[10:11]
	v_add_u32_e32 v194, 0xd7f80, v129
	s_mov_b32 m0, s26
	s_nop 0
	global_load_lds_dwordx4 v194, s[10:11]
	s_waitcnt vmcnt(8) lgkmcnt(0)
	s_barrier
	s_setprio 1
	v_mfma_f32_16x16x32_f16 v[12:15], v[130:133], v[146:149], v[12:15]
	v_mfma_f32_16x16x32_f16 v[8:11], v[138:141], v[146:149], v[8:11]
	v_mfma_f32_16x16x32_f16 v[64:67], v[178:181], v[146:149], v[64:67]
	v_mfma_f32_16x16x32_f16 v[68:71], v[186:189], v[146:149], v[68:71]
	v_mfma_f32_16x16x32_f16 v[4:7], v[130:133], v[154:157], v[4:7]
	v_mfma_f32_16x16x32_f16 v[0:3], v[138:141], v[154:157], v[0:3]
	v_mfma_f32_16x16x32_f16 v[72:75], v[178:181], v[154:157], v[72:75]
	v_mfma_f32_16x16x32_f16 v[76:79], v[186:189], v[154:157], v[76:79]
	v_mfma_f32_16x16x32_f16 v[44:47], v[130:133], v[162:165], v[44:47]
	v_mfma_f32_16x16x32_f16 v[48:51], v[138:141], v[162:165], v[48:51]
	v_mfma_f32_16x16x32_f16 v[80:83], v[178:181], v[162:165], v[80:83]
	v_mfma_f32_16x16x32_f16 v[84:87], v[186:189], v[162:165], v[84:87]
	v_mfma_f32_16x16x32_f16 v[56:59], v[130:133], v[170:173], v[56:59]
	v_mfma_f32_16x16x32_f16 v[60:63], v[138:141], v[170:173], v[60:63]
	v_mfma_f32_16x16x32_f16 v[88:91], v[178:181], v[170:173], v[88:91]
	v_mfma_f32_16x16x32_f16 v[92:95], v[186:189], v[170:173], v[92:95]
	v_mfma_f32_16x16x32_f16 v[12:15], v[134:137], v[150:153], v[12:15]
	v_mfma_f32_16x16x32_f16 v[8:11], v[142:145], v[150:153], v[8:11]
	v_mfma_f32_16x16x32_f16 v[64:67], v[182:185], v[150:153], v[64:67]
	v_mfma_f32_16x16x32_f16 v[68:71], v[190:193], v[150:153], v[68:71]
	v_mfma_f32_16x16x32_f16 v[4:7], v[134:137], v[158:161], v[4:7]
	v_mfma_f32_16x16x32_f16 v[0:3], v[142:145], v[158:161], v[0:3]
	v_mfma_f32_16x16x32_f16 v[72:75], v[182:185], v[158:161], v[72:75]
	v_mfma_f32_16x16x32_f16 v[76:79], v[190:193], v[158:161], v[76:79]
	v_mfma_f32_16x16x32_f16 v[44:47], v[134:137], v[166:169], v[44:47]
	v_mfma_f32_16x16x32_f16 v[48:51], v[142:145], v[166:169], v[48:51]
	v_mfma_f32_16x16x32_f16 v[80:83], v[182:185], v[166:169], v[80:83]
	v_mfma_f32_16x16x32_f16 v[84:87], v[190:193], v[166:169], v[84:87]
	v_mfma_f32_16x16x32_f16 v[56:59], v[134:137], v[174:177], v[56:59]
	v_mfma_f32_16x16x32_f16 v[60:63], v[142:145], v[174:177], v[60:63]
	v_mfma_f32_16x16x32_f16 v[88:91], v[182:185], v[174:177], v[88:91]
	v_mfma_f32_16x16x32_f16 v[92:95], v[190:193], v[174:177], v[92:95]
	s_setprio 0
	s_barrier
	ds_read_b128 v[130:133], v224
	ds_read_b128 v[134:137], v224 offset:1024
	ds_read_b128 v[138:141], v224 offset:2048
	ds_read_b128 v[142:145], v224 offset:3072
	ds_read_b128 v[178:181], v229
	ds_read_b128 v[182:185], v229 offset:1024
	ds_read_b128 v[186:189], v229 offset:2048
	ds_read_b128 v[190:193], v229 offset:3072
	ds_read_b128 v[146:149], v225
	ds_read_b128 v[150:153], v225 offset:1024
	ds_read_b128 v[154:157], v226
	ds_read_b128 v[158:161], v226 offset:1024
	ds_read_b128 v[162:165], v227
	ds_read_b128 v[166:169], v227 offset:1024
	ds_read_b128 v[170:173], v228
	ds_read_b128 v[174:177], v228 offset:1024
	v_readlane_b32 s12, v248, s9
	s_mov_b32 m0, s27
	s_nop 1
	v_add_u32_e32 v251, s12, v249
	global_load_lds_dwordx4 v251, s[18:19]
	v_add_u32_e32 v251, s12, v250
	s_mov_b32 m0, s28
	s_nop 0
	global_load_lds_dwordx4 v251, s[18:19]
	s_waitcnt vmcnt(8) lgkmcnt(0)
	s_barrier
	s_setprio 1
	v_mfma_f32_16x16x32_f16 v[124:127], v[130:133], v[146:149], v[124:127]
	v_mfma_f32_16x16x32_f16 v[120:123], v[138:141], v[146:149], v[120:123]
	v_mfma_f32_16x16x32_f16 v[52:55], v[178:181], v[146:149], v[52:55]
	v_mfma_f32_16x16x32_f16 v[40:43], v[186:189], v[146:149], v[40:43]
	v_mfma_f32_16x16x32_f16 v[116:119], v[130:133], v[154:157], v[116:119]
	v_mfma_f32_16x16x32_f16 v[112:115], v[138:141], v[154:157], v[112:115]
	v_mfma_f32_16x16x32_f16 v[36:39], v[178:181], v[154:157], v[36:39]
	v_mfma_f32_16x16x32_f16 v[32:35], v[186:189], v[154:157], v[32:35]
	v_mfma_f32_16x16x32_f16 v[108:111], v[130:133], v[162:165], v[108:111]
	v_mfma_f32_16x16x32_f16 v[104:107], v[138:141], v[162:165], v[104:107]
	v_mfma_f32_16x16x32_f16 v[28:31], v[178:181], v[162:165], v[28:31]
	v_mfma_f32_16x16x32_f16 v[24:27], v[186:189], v[162:165], v[24:27]
	v_mfma_f32_16x16x32_f16 v[100:103], v[130:133], v[170:173], v[100:103]
	v_mfma_f32_16x16x32_f16 v[96:99], v[138:141], v[170:173], v[96:99]
	v_mfma_f32_16x16x32_f16 v[20:23], v[178:181], v[170:173], v[20:23]
	v_mfma_f32_16x16x32_f16 v[16:19], v[186:189], v[170:173], v[16:19]
	v_mfma_f32_16x16x32_f16 v[124:127], v[134:137], v[150:153], v[124:127]
	v_mfma_f32_16x16x32_f16 v[120:123], v[142:145], v[150:153], v[120:123]
	v_mfma_f32_16x16x32_f16 v[52:55], v[182:185], v[150:153], v[52:55]
	v_mfma_f32_16x16x32_f16 v[40:43], v[190:193], v[150:153], v[40:43]
	v_mfma_f32_16x16x32_f16 v[116:119], v[134:137], v[158:161], v[116:119]
	v_mfma_f32_16x16x32_f16 v[112:115], v[142:145], v[158:161], v[112:115]
	v_mfma_f32_16x16x32_f16 v[36:39], v[182:185], v[158:161], v[36:39]
	v_mfma_f32_16x16x32_f16 v[32:35], v[190:193], v[158:161], v[32:35]
	v_mfma_f32_16x16x32_f16 v[108:111], v[134:137], v[166:169], v[108:111]
	v_mfma_f32_16x16x32_f16 v[104:107], v[142:145], v[166:169], v[104:107]
	v_mfma_f32_16x16x32_f16 v[28:31], v[182:185], v[166:169], v[28:31]
	v_mfma_f32_16x16x32_f16 v[24:27], v[190:193], v[166:169], v[24:27]
	v_mfma_f32_16x16x32_f16 v[100:103], v[134:137], v[174:177], v[100:103]
	v_mfma_f32_16x16x32_f16 v[96:99], v[142:145], v[174:177], v[96:99]
	v_mfma_f32_16x16x32_f16 v[20:23], v[182:185], v[174:177], v[20:23]
	v_mfma_f32_16x16x32_f16 v[16:19], v[190:193], v[174:177], v[16:19]
	s_setprio 0
	s_barrier
	ds_read_b128 v[146:149], v230
	ds_read_b128 v[150:153], v230 offset:1024
	ds_read_b128 v[154:157], v231
	ds_read_b128 v[158:161], v231 offset:1024
	ds_read_b128 v[162:165], v232
	ds_read_b128 v[166:169], v232 offset:1024
	ds_read_b128 v[170:173], v233
	ds_read_b128 v[174:177], v233 offset:1024
	s_mov_b32 m0, s37
	v_add_u32_e32 v194, 0x48000, v129
	global_load_lds_dwordx4 v129, s[10:11]
	s_mov_b32 m0, s38
	s_add_i32 s12, s8, 3
	global_load_lds_dwordx4 v194, s[10:11]
	v_readlane_b32 s13, v248, s12
	s_mov_b32 m0, s39
	s_nop 1
	v_add_u32_e32 v194, s13, v206
	global_load_lds_dwordx4 v194, s[18:19]
	v_add_u32_e32 v194, s13, v213
	s_mov_b32 m0, s40
	s_nop 0
	global_load_lds_dwordx4 v194, s[18:19]
	s_mov_b32 m0, s41
	v_add_u32_e32 v194, 0x90000, v129
	global_load_lds_dwordx4 v194, s[10:11]
	v_add_u32_e32 v194, 0xd8000, v129
	s_mov_b32 m0, s42
	s_nop 0
	global_load_lds_dwordx4 v194, s[10:11]
	s_waitcnt vmcnt(8) lgkmcnt(0)
	s_barrier
	s_setprio 1
	v_mfma_f32_16x16x32_f16 v[12:15], v[130:133], v[146:149], v[12:15]
	v_mfma_f32_16x16x32_f16 v[8:11], v[138:141], v[146:149], v[8:11]
	v_mfma_f32_16x16x32_f16 v[64:67], v[178:181], v[146:149], v[64:67]
	v_mfma_f32_16x16x32_f16 v[68:71], v[186:189], v[146:149], v[68:71]
	v_mfma_f32_16x16x32_f16 v[4:7], v[130:133], v[154:157], v[4:7]
	v_mfma_f32_16x16x32_f16 v[0:3], v[138:141], v[154:157], v[0:3]
	v_mfma_f32_16x16x32_f16 v[72:75], v[178:181], v[154:157], v[72:75]
	v_mfma_f32_16x16x32_f16 v[76:79], v[186:189], v[154:157], v[76:79]
	v_mfma_f32_16x16x32_f16 v[44:47], v[130:133], v[162:165], v[44:47]
	v_mfma_f32_16x16x32_f16 v[48:51], v[138:141], v[162:165], v[48:51]
	v_mfma_f32_16x16x32_f16 v[80:83], v[178:181], v[162:165], v[80:83]
	v_mfma_f32_16x16x32_f16 v[84:87], v[186:189], v[162:165], v[84:87]
	v_mfma_f32_16x16x32_f16 v[56:59], v[130:133], v[170:173], v[56:59]
	v_mfma_f32_16x16x32_f16 v[60:63], v[138:141], v[170:173], v[60:63]
	v_mfma_f32_16x16x32_f16 v[88:91], v[178:181], v[170:173], v[88:91]
	v_mfma_f32_16x16x32_f16 v[92:95], v[186:189], v[170:173], v[92:95]
	v_mfma_f32_16x16x32_f16 v[12:15], v[134:137], v[150:153], v[12:15]
	v_mfma_f32_16x16x32_f16 v[8:11], v[142:145], v[150:153], v[8:11]
	v_mfma_f32_16x16x32_f16 v[64:67], v[182:185], v[150:153], v[64:67]
	v_mfma_f32_16x16x32_f16 v[68:71], v[190:193], v[150:153], v[68:71]
	v_mfma_f32_16x16x32_f16 v[4:7], v[134:137], v[158:161], v[4:7]
	v_mfma_f32_16x16x32_f16 v[0:3], v[142:145], v[158:161], v[0:3]
	v_mfma_f32_16x16x32_f16 v[72:75], v[182:185], v[158:161], v[72:75]
	v_mfma_f32_16x16x32_f16 v[76:79], v[190:193], v[158:161], v[76:79]
	v_mfma_f32_16x16x32_f16 v[44:47], v[134:137], v[166:169], v[44:47]
	v_mfma_f32_16x16x32_f16 v[48:51], v[142:145], v[166:169], v[48:51]
	v_mfma_f32_16x16x32_f16 v[80:83], v[182:185], v[166:169], v[80:83]
	v_mfma_f32_16x16x32_f16 v[84:87], v[190:193], v[166:169], v[84:87]
	v_mfma_f32_16x16x32_f16 v[56:59], v[134:137], v[174:177], v[56:59]
	v_mfma_f32_16x16x32_f16 v[60:63], v[142:145], v[174:177], v[60:63]
	v_mfma_f32_16x16x32_f16 v[88:91], v[182:185], v[174:177], v[88:91]
	v_mfma_f32_16x16x32_f16 v[92:95], v[190:193], v[174:177], v[92:95]
	s_setprio 0
	s_addk_i32 s7, 0x100
	s_cmp_lt_u32 s8, 32
	s_mov_b32 s8, s9
	s_barrier
	s_cbranch_scc1 .LBB1_82
	ds_read_b128 v[132:135], v219 offset:32768
	ds_read_b128 v[136:139], v219 offset:33792
	ds_read_b128 v[140:143], v219 offset:34816
	ds_read_b128 v[144:147], v219 offset:35840
	ds_read_b128 v[128:131], v220
	ds_read_b128 v[148:151], v220 offset:1024
	ds_read_b128 v[152:155], v221
	ds_read_b128 v[156:159], v221 offset:1024
	ds_read_b128 v[188:191], v222
	ds_read_b128 v[192:195], v222 offset:1024
	ds_read_b128 v[196:199], v223
	ds_read_b128 v[200:203], v223 offset:1024
	s_setprio 2
	s_lshl_b32 s3, s50, 9
	s_add_i32 s3, s47, s3
	s_add_i32 s3, s3, 0x10380
	s_mov_b32 m0, s43
	v_add_u32_e32 v160, s3, v206
	global_load_lds_dwordx4 v160, s[18:19]
	v_add_u32_e32 v160, s3, v213
	s_mov_b32 m0, s44
	s_nop 0
	global_load_lds_dwordx4 v160, s[18:19]
	s_setprio 0
	s_waitcnt vmcnt(8)
	s_waitcnt lgkmcnt(0)
	s_barrier
	s_waitcnt lgkmcnt(0)
	s_setprio 1
	s_waitcnt lgkmcnt(0)
	v_mfma_f32_16x16x32_f16 v[124:127], v[132:135], v[128:131], v[124:127]
	v_mfma_f32_16x16x32_f16 v[120:123], v[140:143], v[128:131], v[120:123]
	v_mfma_f32_16x16x32_f16 v[116:119], v[132:135], v[152:155], v[116:119]
	v_mfma_f32_16x16x32_f16 v[112:115], v[140:143], v[152:155], v[112:115]
	v_mfma_f32_16x16x32_f16 v[108:111], v[132:135], v[188:191], v[108:111]
	v_mfma_f32_16x16x32_f16 v[104:107], v[140:143], v[188:191], v[104:107]
	v_mfma_f32_16x16x32_f16 v[100:103], v[132:135], v[196:199], v[100:103]
	v_mfma_f32_16x16x32_f16 v[96:99], v[140:143], v[196:199], v[96:99]
	v_mfma_f32_16x16x32_f16 v[160:163], v[136:139], v[148:151], v[124:127]
	v_mfma_f32_16x16x32_f16 v[164:167], v[144:147], v[148:151], v[120:123]
	v_mfma_f32_16x16x32_f16 v[168:171], v[136:139], v[156:159], v[116:119]
	v_mfma_f32_16x16x32_f16 v[172:175], v[144:147], v[156:159], v[112:115]
	v_mfma_f32_16x16x32_f16 v[176:179], v[136:139], v[192:195], v[108:111]
	v_mfma_f32_16x16x32_f16 v[180:183], v[144:147], v[192:195], v[104:107]
	v_mfma_f32_16x16x32_f16 v[100:103], v[136:139], v[200:203], v[100:103]
	v_mfma_f32_16x16x32_f16 v[184:187], v[144:147], v[200:203], v[96:99]
	s_setprio 0
	s_barrier
	ds_read_b128 v[104:107], v219 offset:49152
	ds_read_b128 v[108:111], v219 offset:50176
	ds_read_b128 v[116:119], v219 offset:51200
	ds_read_b128 v[236:239], v219 offset:52224
	s_waitcnt lgkmcnt(0)
	s_barrier
	s_waitcnt lgkmcnt(0)
	s_setprio 1
	s_waitcnt lgkmcnt(0)
	v_mfma_f32_16x16x32_f16 v[52:55], v[104:107], v[128:131], v[52:55]
	v_mfma_f32_16x16x32_f16 v[40:43], v[116:119], v[128:131], v[40:43]
	v_mfma_f32_16x16x32_f16 v[36:39], v[104:107], v[152:155], v[36:39]
	v_mfma_f32_16x16x32_f16 v[32:35], v[116:119], v[152:155], v[32:35]
	v_mfma_f32_16x16x32_f16 v[28:31], v[104:107], v[188:191], v[28:31]
	v_mfma_f32_16x16x32_f16 v[24:27], v[116:119], v[188:191], v[24:27]
	v_mfma_f32_16x16x32_f16 v[20:23], v[104:107], v[196:199], v[20:23]
	v_mfma_f32_16x16x32_f16 v[16:19], v[116:119], v[196:199], v[16:19]
	v_mfma_f32_16x16x32_f16 v[52:55], v[108:111], v[148:151], v[52:55]
	v_mfma_f32_16x16x32_f16 v[40:43], v[236:239], v[148:151], v[40:43]
	v_mfma_f32_16x16x32_f16 v[36:39], v[108:111], v[156:159], v[36:39]
	v_mfma_f32_16x16x32_f16 v[32:35], v[236:239], v[156:159], v[32:35]
	v_mfma_f32_16x16x32_f16 v[28:31], v[108:111], v[192:195], v[28:31]
	v_mfma_f32_16x16x32_f16 v[24:27], v[236:239], v[192:195], v[24:27]
	v_mfma_f32_16x16x32_f16 v[96:99], v[108:111], v[200:203], v[20:23]
	v_mfma_f32_16x16x32_f16 v[16:19], v[236:239], v[200:203], v[16:19]
	s_setprio 0
	s_barrier
	ds_read_b128 v[20:23], v220 offset:16384
	ds_read_b128 v[148:151], v220 offset:17408
	ds_read_b128 v[152:155], v221 offset:16384
	ds_read_b128 v[156:159], v221 offset:17408
	ds_read_b128 v[188:191], v222 offset:16384
	ds_read_b128 v[192:195], v222 offset:17408
	ds_read_b128 v[196:199], v223 offset:16384
	ds_read_b128 v[200:203], v223 offset:17408
	s_waitcnt vmcnt(4)
	s_waitcnt lgkmcnt(0)
	s_barrier
	s_waitcnt lgkmcnt(0)
	s_setprio 1
	s_waitcnt lgkmcnt(0)
	v_mfma_f32_16x16x32_f16 v[0:3], v[140:143], v[152:155], v[0:3]
	v_mfma_f32_16x16x32_f16 v[124:127], v[144:147], v[156:159], v[0:3]
	v_mfma_f32_16x16x32_f16 v[0:3], v[132:135], v[188:191], v[44:47]
	v_mfma_f32_16x16x32_f16 v[128:131], v[136:139], v[192:195], v[0:3]
	v_mfma_f32_16x16x32_f16 v[0:3], v[140:143], v[188:191], v[48:51]
	v_mfma_f32_16x16x32_f16 v[48:51], v[144:147], v[192:195], v[0:3]
	v_mfma_f32_16x16x32_f16 v[0:3], v[132:135], v[196:199], v[56:59]
	v_mfma_f32_16x16x32_f16 v[12:15], v[132:135], v[20:23], v[12:15]
	v_mfma_f32_16x16x32_f16 v[8:11], v[140:143], v[20:23], v[8:11]
	v_mfma_f32_16x16x32_f16 v[4:7], v[132:135], v[152:155], v[4:7]
	v_mfma_f32_16x16x32_f16 v[56:59], v[136:139], v[200:203], v[0:3]
	v_mfma_f32_16x16x32_f16 v[0:3], v[140:143], v[196:199], v[60:63]
	v_mfma_f32_16x16x32_f16 v[112:115], v[136:139], v[148:151], v[12:15]
	v_mfma_f32_16x16x32_f16 v[8:11], v[144:147], v[148:151], v[8:11]
	v_mfma_f32_16x16x32_f16 v[120:123], v[136:139], v[156:159], v[4:7]
	v_mfma_f32_16x16x32_f16 v[60:63], v[144:147], v[200:203], v[0:3]
	s_setprio 0
	s_setprio 1
	v_mfma_f32_16x16x32_f16 v[0:3], v[104:107], v[20:23], v[64:67]
	v_mfma_f32_16x16x32_f16 v[132:135], v[108:111], v[148:151], v[0:3]
	v_mfma_f32_16x16x32_f16 v[0:3], v[116:119], v[20:23], v[68:71]
	v_mfma_f32_16x16x32_f16 v[136:139], v[236:239], v[148:151], v[0:3]
	v_mfma_f32_16x16x32_f16 v[0:3], v[104:107], v[152:155], v[72:75]
	v_mfma_f32_16x16x32_f16 v[140:143], v[108:111], v[156:159], v[0:3]
	v_mfma_f32_16x16x32_f16 v[0:3], v[116:119], v[152:155], v[76:79]
	v_mfma_f32_16x16x32_f16 v[144:147], v[236:239], v[156:159], v[0:3]
	v_mfma_f32_16x16x32_f16 v[0:3], v[104:107], v[188:191], v[80:83]
	v_mfma_f32_16x16x32_f16 v[80:83], v[108:111], v[192:195], v[0:3]
	v_mfma_f32_16x16x32_f16 v[0:3], v[116:119], v[188:191], v[84:87]
	v_mfma_f32_16x16x32_f16 v[148:151], v[236:239], v[192:195], v[0:3]
	v_mfma_f32_16x16x32_f16 v[0:3], v[104:107], v[196:199], v[88:91]
	v_mfma_f32_16x16x32_f16 v[152:155], v[108:111], v[200:203], v[0:3]
	v_mfma_f32_16x16x32_f16 v[0:3], v[116:119], v[196:199], v[92:95]
	v_mfma_f32_16x16x32_f16 v[156:159], v[236:239], v[200:203], v[0:3]
	s_setprio 0
	s_add_i32 s49, s49, s17
	s_cmpk_lt_i32 s49, 0x1c8
	s_cselect_b64 s[6:7], -1, 0
	s_cmpk_gt_i32 s49, 0x1c7
	s_cselect_b64 s[12:13], -1, 0
	s_and_b64 vcc, exec, s[12:13]
	s_mov_b32 s54, s2
	s_mov_b32 s53, s51
	s_mov_b32 s55, s52
	s_barrier
	s_cbranch_vccnz .LBB1_100
	s_cmpk_lt_i32 s49, 0x148
	s_cbranch_scc1 .LBB1_88
	s_cmpk_lt_u32 s49, 0x1a0
	s_cbranch_scc1 .LBB1_89
	s_cmpk_lt_u32 s49, 0x1b8
	s_cbranch_scc1 .LBB1_90
	s_cmpk_lt_u32 s49, 0x1c0
	s_cselect_b32 s47, s45, 0xfffffe40
	s_cselect_b32 s48, 3, 4
	s_mov_b32 s3, 1
	s_cmp_lt_i32 s48, 1
	s_movk_i32 s53, 0x64
	s_cbranch_scc0 .LBB1_91
	s_branch .LBB1_99
